# v32: v31 + DSA selection-mask tile fetched by 2 dwordx4 LDS-DMA pieces (4 waves/step) instead of 8 dword pieces per tile
# speedup vs baseline: 1.0079x; 1.0008x over previous
; #define LAS __attribute__((address_space(3)))
; __device__ __forceinline__ int lane_id_v() { int l; asm volatile("v_mbcnt_lo_u32_b32 %0, -1, 0\n\tv_mbcnt_hi_u32_b32 %0, -1, %0" : "=v"(l)); return l & 63; }
; template <int MODE, int DQK, int DV>
; __device__ __forceinline__ void attn_pass(LAS unsigned char* lds, const Tens& T, size_t rowbase, int q0, f32x16 (&o)[DV / 32], float& l_out, const int wave, QPre* qp = nullptr) {
;     ...
;     const unsigned cvo = (unsigned)lane * 32u, mvo = (unsigned)(wave * 64 + lane) * 4u;
;     const char* const ubK = (const char*)(T.K + rowbase * (size_t)T.ldk);
;     const char* const ubK2 = (MODE == AM_MLA) ? (const char*)(T.K2 + rowbase * (size_t)T.ldk2) : nullptr;
;     const char* const ubV = (const char*)(T.V + rowbase * (size_t)T.ldv);
;     const char* const ubC = (MODE == AM_FOX) ? (const char*)(T.lc + rowbase * 8) : nullptr;
;     const char* const ubM = (MODE == AM_DSA) ? (const char*)(T.mask + ((rowbase / S * 128) * (size_t)S + q0) * 2) : nullptr;
; template <int PH>
; __device__ __forceinline__ void mk_body(const Args& a) {
;     ...
;     if (IN(19)) {
;         att::QPre qp{nullptr, 0u, false};
;         for (;;) {
;             const int u = att::next_unit_pre(qp, ctl + CW_Q + 1 * 512, 256, lds, att::OFF_MISC, wave);
;             if (u < 0) break;
;             const int b = u >> 8, h = (u >> 5) & 7, qb = 31 - (u & 31);
;             { const int t_ = wave * 64 + lane_id_v();
;               if (t_ <= 128) ((LAS float*)(lds + att::OFF_LUT))[t_] = (t_ < 128) ? (t5[bucket_tab[t_] * 8 + h] - t5[31 * 8 + h]) * att::LOG2E : 0.f;
;               if (t_ >= 192 && t_ < 256) { const int e_ = (t_ - 192) >> 2, c_ = t_ & 3; ((LAS float*)(lds + att::OFF_LUT + 768))[t_ - 192] = ((e_ >> c_) & 1) ? 0.f : -INFINITY; } }
;             att::Tens T{};
;             T.Q = y0 + Y0_DQ + h * 64; T.ldq = Y0P; T.K = y0 + Y0_DK + h * 64; T.ldk = Y0P; T.V = y0 + Y0_DV + h * 64; T.ldv = Y0P;
;             T.mask = maskg; T.scale2 = 0.125f * att::LOG2E;
;             att::f32x16 o[2]; float l;
;             att::attn_pass<att::AM_DSA, 64, 64>(lds, T, (size_t)b * S, qb * 256, o, l, wave, &qp);
.LBB0_1592:
	v_readlane_b32 s2, v254, 0
	v_readlane_b32 s3, v254, 1
	s_cmp_lt_i32 s2, 20
	s_cselect_b64 s[0:1], -1, 0
	s_cmp_gt_i32 s3, 19
	s_cselect_b64 s[2:3], -1, 0
	s_and_b64 s[0:1], s[0:1], s[2:3]
	s_andn2_b64 vcc, exec, s[0:1]
	s_waitcnt lgkmcnt(0)
	s_barrier
	s_cbranch_vccnz .LBB0_1706
	v_readlane_b32 s99, v254, 24
	s_nop 3
	s_and_b32 s100, s99, 1
	s_lshl_b32 s100, s100, 10
	v_mbcnt_lo_u32_b32 v155, -1, 0
	v_mbcnt_hi_u32_b32 v155, -1, v155
	v_lshlrev_b32_e32 v155, 4, v155
	v_add_u32_e32 v155, s100, v155
	s_lshl_b32 s101, s99, 8
	s_sub_i32 s100, s100, s101
	s_lshr_b32 s101, s99, 1
	s_add_u32 s6, s54, 0x8800
	s_addc_u32 s7, s55, 0
	s_add_u32 s86, s54, 0x3900000
	s_addc_u32 s87, s55, 0
	s_cmpk_eq_i32 s90, 0xc0
	s_cselect_b64 s[0:1], -1, 0
	s_add_u32 s92, s54, 0x18800c00
	s_addc_u32 s40, s55, 0
	s_add_u32 s41, s54, 0x18801000
	s_addc_u32 s44, s55, 0
	v_writelane_b32 v254, s0, 57
	s_add_u32 s45, s54, 0x18801400
	s_addc_u32 s46, s55, 0
	v_writelane_b32 v254, s1, 58
	s_add_u32 s47, s54, 0x14800000
	v_readlane_b32 s0, v254, 24
	s_addc_u32 s48, s55, 0
	s_lshl_b32 s65, s0, 8
	s_lshl_b32 s49, s0, 5
	s_add_i32 s72, s65, 0
	s_lshl_b32 s64, s0, 3
	s_lshl_b32 s66, s0, 10
	s_mov_b32 s13, 0
	s_add_i32 s67, s72, 0x18000
	s_add_i32 s68, s72, 0x18800
	s_add_i32 s69, s72, 0x19000
	s_add_i32 s70, s72, 0x19800
	s_add_i32 s71, s72, 0x1a000
	s_add_i32 s72, s72, 0x1a800
	s_add_i32 s73, s49, 0xffffff80
	v_mov_b32_e32 v66, 0
	v_mov_b32_e32 v103, 0
	s_movk_i32 s74, 0x100
	v_mov_b32_e32 v88, 1
	s_mov_b32 s14, 0x3e38aa3b
	s_movk_i32 s76, 0x7fff
	s_mov_b32 s78, 0x7060302
	s_add_i32 s79, 0, 0x1fb00
	s_mov_b32 s80, 0x47800000
	v_mov_b32_e32 v89, 0xff800000
	v_mov_b32_e32 v90, 0x4280
	v_mov_b32_e32 v91, 0x3f80
	v_mov_b32_e32 v92, 0x3f803f80
	v_mov_b32_e32 v93, 0x80
	v_mov_b32_e32 v94, 0
	s_branch .LBB0_1595

; template <int MODE, int DQK, int DV>
; __device__ __forceinline__ void attn_pass(LAS unsigned char* lds, const Tens& T, size_t rowbase, int q0, f32x16 (&o)[DV / 32], float& l_out, const int wave, QPre* qp = nullptr) {
;     ...
;         const bf16* qp = T.Q + (rowbase + tq) * (size_t)T.ldq + 8 * h;
; #pragma unroll
;         for (int s = 0; s < NSTEP; ++s) qf[s] = *(const bf16x8*)(qp + 16 * s);
;     }
;     {
;         f32x4 c0 = {1.f, 1.f, 1.f, 1.f}, c1 = c0, s0 = {0.f, 0.f, 0.f, 0.f}, s1 = s0;
;         if (MODE == AM_MLA) {
;             c0 = *(const f32x4*)(T.rcos + tq * 16 + 8 * h); c1 = *(const f32x4*)(T.rcos + tq * 16 + 8 * h + 4);
;             s0 = *(const f32x4*)(T.rsin + tq * 16 + 8 * h); s1 = *(const f32x4*)(T.rsin + tq * 16 + 8 * h + 4);
;         }
; #pragma unroll
;         for (int s = 0; s < NSTEP; ++s) {
;             if (MODE == AM_MLA && s == NSTEP - 1) continue;
;             bf16x8 a = qf[s];
;             if (MODE == AM_MLA && s == NSTEP - 2) {
;                 bf16x8 b2 = qf[NSTEP - 1];
; #pragma unroll
;                 for (int j = 0; j < 8; ++j) {
;                     const float x1 = __uint_as_float(((unsigned)(unsigned short)a[j]) << 16), x2 = __uint_as_float(((unsigned)(unsigned short)b2[j]) << 16);
;                     const float cs = j < 4 ? c0[j & 3] : c1[j & 3], sn = j < 4 ? s0[j & 3] : s1[j & 3];
;                     a[j] = (short)f2bf((x1 * cs - x2 * sn) * T.scale2); b2[j] = (short)f2bf((x2 * cs + x1 * sn) * T.scale2);
;                 }
;                 qf[NSTEP - 1] = b2;
;             } else {
; #pragma unroll
;                 for (int j = 0; j < 8; ++j) a[j] = (short)f2bf(__uint_as_float(((unsigned)(unsigned short)a[j]) << 16) * T.scale2);
;             }
;             qf[s] = a;
;         }
;     }
;     float ct2 = 0.f, bq = 0.f;
;     if (MODE == AM_FOX) {
;         ct2 = T.lc[(rowbase + tq) * 8] * LOG2E;
;         float qs = 0.f;
; #pragma unroll
;         for (int s = 0; s < NSTEP; ++s)
; #pragma unroll
;             for (int j = 0; j < 8; ++j) { const float v = __uint_as_float(((unsigned)(unsigned short)qf[s][j]) << 16); qs = fmaf(v, v, qs); }
;         qs = sum32f(qs);
;         bq = sqrtf(qs) * T.kmaxn * 1.001f + 1.0f;
;     }
;     const LAS float* lut = (const LAS float*)(lds + OFF_LUT);
;     const int dk_key = 8 * wave + (lane >> 3), dk_col = ((lane & 7) ^ ((dk_key >> 1) & 7)) * 8;
.LBB0_1618:
	s_lshr_b32 s12, s8, 8
	s_lshl_b32 s0, s0, 8
	s_add_u32 s16, s6, s0
	s_addc_u32 s17, s7, 0
	s_lshl_b32 s81, s1, 6
	s_lshl_b32 s0, s1, 7
	s_add_u32 s10, s92, s0
	s_addc_u32 s11, s40, 0
	s_add_u32 s1, s41, s0
	s_addc_u32 s2, s44, 0
	s_add_u32 s3, s45, s0
	s_addc_u32 s4, s46, 0
	s_not_b32 s0, s8
	s_lshl_b32 s0, s0, 8
	s_and_b32 s82, s0, 0x1f00
	v_mbcnt_lo_u32_b32 v28, -1, 0
	v_mbcnt_hi_u32_b32 v28, -1, v28
	s_add_i32 s83, s82, s49
	v_and_b32_e32 v29, 31, v28
	s_lshl_b64 s[18:19], s[12:13], 13
	v_or_b32_e32 v0, s83, v29
	v_mov_b32_e32 v1, v66
	v_lshl_add_u64 v[0:1], s[18:19], 0, v[0:1]
	v_mov_b64_e32 v[2:3], s[10:11]
	s_movk_i32 s0, 0x1c00
	v_bfe_u32 v30, v28, 5, 1
	v_mad_u64_u32 v[2:3], s[8:9], v0, s0, v[2:3]
	v_mad_u32_u24 v3, v1, s0, v3
	v_lshlrev_b32_e32 v0, 4, v30
	v_mov_b32_e32 v1, v66
	v_lshl_add_u64 v[12:13], v[2:3], 0, v[0:1]
	global_load_dwordx4 v[0:3], v[12:13], off
	global_load_dwordx4 v[4:7], v[12:13], off offset:32
	global_load_dwordx4 v[8:11], v[12:13], off offset:64
	s_movk_i32 s5, 0xe00
	global_load_dwordx4 v[12:15], v[12:13], off offset:96
	s_add_i32 s0, s82, 0x100
	s_lshl_b64 s[8:9], s[12:13], 23
	s_mul_i32 s11, s12, 0x3800000
	s_mul_hi_u32 s10, s12, 0x3800000
	v_and_b32_e32 v31, 63, v28
	v_lshlrev_b32_e32 v106, 2, v30
	v_lshlrev_b32_e32 v105, 3, v29
	s_mov_b32 s84, 4
	v_mov_b32_e32 v65, v66
	v_mov_b32_e32 v67, v66
	v_mov_b32_e32 v70, v66
	v_mov_b32_e32 v71, v66
	v_or_b32_e32 v107, 8, v106
	v_or_b32_e32 v108, 16, v106
	v_or_b32_e32 v109, 24, v106
	v_mov_b32_e32 v111, 0
	v_mov_b32_e32 v112, 0xc2800000
	v_mov_b32_e32 v103, 0
	s_mov_b64 s[26:27], 0
	s_waitcnt vmcnt(0)
	v_and_b32_e32 v17, 0xffff0000, v0
	v_lshlrev_b32_e32 v16, 16, v0
	v_and_b32_e32 v19, 0xffff0000, v1
	v_lshlrev_b32_e32 v18, 16, v1
	v_and_b32_e32 v1, 0xffff0000, v2
	v_lshlrev_b32_e32 v0, 16, v2
	v_and_b32_e32 v21, 0xffff0000, v3
	v_lshlrev_b32_e32 v20, 16, v3
	v_and_b32_e32 v3, 0xffff0000, v4
	v_lshlrev_b32_e32 v2, 16, v4
	v_and_b32_e32 v25, 0xffff0000, v7
	v_lshlrev_b32_e32 v24, 16, v7
	v_pk_mul_f32 v[20:21], v[20:21], s[14:15] op_sel_hi:[1,0]
	v_pk_mul_f32 v[2:3], v[2:3], s[14:15] op_sel_hi:[1,0]
	v_and_b32_e32 v23, 0xffff0000, v5
	v_lshlrev_b32_e32 v22, 16, v5
	v_and_b32_e32 v5, 0xffff0000, v6
	v_lshlrev_b32_e32 v4, 16, v6
	v_and_b32_e32 v7, 0xffff0000, v8
	v_lshlrev_b32_e32 v6, 16, v8
	v_and_b32_e32 v27, 0xffff0000, v9
	v_lshlrev_b32_e32 v26, 16, v9
	v_and_b32_e32 v9, 0xffff0000, v10
	v_lshlrev_b32_e32 v8, 16, v10
	v_pk_mul_f32 v[16:17], v[16:17], s[14:15] op_sel_hi:[1,0]
	v_pk_mul_f32 v[24:25], v[24:25], s[14:15] op_sel_hi:[1,0]
	v_bfe_u32 v10, v21, 16, 1
	v_bfe_u32 v32, v20, 16, 1
	v_bfe_u32 v45, v3, 16, 1
	v_bfe_u32 v46, v2, 16, 1
	v_pk_mul_f32 v[18:19], v[18:19], s[14:15] op_sel_hi:[1,0]
	v_pk_mul_f32 v[0:1], v[0:1], s[14:15] op_sel_hi:[1,0]
	v_pk_mul_f32 v[4:5], v[4:5], s[14:15] op_sel_hi:[1,0]
	v_pk_mul_f32 v[6:7], v[6:7], s[14:15] op_sel_hi:[1,0]
	v_bfe_u32 v38, v16, 16, 1
	v_bfe_u32 v39, v25, 16, 1
	v_add3_u32 v20, v20, v32, s76
	v_add3_u32 v10, v21, v10, s76
	v_add3_u32 v21, v2, v46, s76
	v_add3_u32 v32, v3, v45, s76
	v_and_b32_e32 v3, 0xffff0000, v11
	v_lshlrev_b32_e32 v2, 16, v11
	v_pk_mul_f32 v[26:27], v[26:27], s[14:15] op_sel_hi:[1,0]
	v_bfe_u32 v33, v1, 16, 1
	v_bfe_u32 v34, v0, 16, 1
	v_bfe_u32 v35, v19, 16, 1
	v_bfe_u32 v36, v18, 16, 1
	v_bfe_u32 v37, v17, 16, 1
	v_bfe_u32 v41, v5, 16, 1
	v_bfe_u32 v42, v4, 16, 1
	v_add3_u32 v16, v16, v38, s76
	v_add3_u32 v25, v25, v39, s76
	v_pk_mul_f32 v[2:3], v[2:3], s[14:15] op_sel_hi:[1,0]
	v_bfe_u32 v38, v7, 16, 1
	v_bfe_u32 v39, v6, 16, 1
	v_add3_u32 v17, v17, v37, s76
	v_add3_u32 v18, v18, v36, s76
	v_add3_u32 v19, v19, v35, s76
	v_add3_u32 v34, v0, v34, s76
	v_add3_u32 v33, v1, v33, s76
	v_add3_u32 v35, v4, v42, s76
	v_add3_u32 v36, v5, v41, s76
	v_pk_mul_f32 v[0:1], v[8:9], s[14:15] op_sel_hi:[1,0]
	v_bfe_u32 v4, v3, 16, 1
	v_bfe_u32 v5, v2, 16, 1
	v_bfe_u32 v11, v27, 16, 1
	v_bfe_u32 v37, v26, 16, 1
	v_add3_u32 v39, v6, v39, s76
	v_add3_u32 v38, v7, v38, s76
	v_and_b32_e32 v7, 0xffff0000, v15
	v_lshlrev_b32_e32 v6, 16, v15
	v_bfe_u32 v8, v1, 16, 1
	v_bfe_u32 v9, v0, 16, 1
	v_add3_u32 v26, v26, v37, s76
	v_add3_u32 v11, v27, v11, s76
	v_add3_u32 v27, v2, v5, s76
	v_add3_u32 v37, v3, v4, s76
	v_and_b32_e32 v3, 0xffff0000, v13
	v_lshlrev_b32_e32 v2, 16, v13
	v_and_b32_e32 v5, 0xffff0000, v14
	v_lshlrev_b32_e32 v4, 16, v14
	v_pk_mul_f32 v[6:7], v[6:7], s[14:15] op_sel_hi:[1,0]
	v_bfe_u32 v40, v24, 16, 1
	v_add3_u32 v9, v0, v9, s76
	v_add3_u32 v8, v1, v8, s76
	v_and_b32_e32 v1, 0xffff0000, v12
	v_lshlrev_b32_e32 v0, 16, v12
	v_pk_mul_f32 v[2:3], v[2:3], s[14:15] op_sel_hi:[1,0]
	v_pk_mul_f32 v[4:5], v[4:5], s[14:15] op_sel_hi:[1,0]
	v_bfe_u32 v12, v7, 16, 1
	v_add3_u32 v24, v24, v40, s76
	v_bfe_u32 v13, v6, 16, 1
	v_bfe_u32 v15, v4, 16, 1
	v_bfe_u32 v40, v3, 16, 1
	v_add3_u32 v7, v7, v12, s76
	v_bfe_u32 v12, v28, 3, 3
	v_bfe_u32 v14, v5, 16, 1
	v_add3_u32 v3, v3, v40, s76
	v_add3_u32 v4, v4, v15, s76
	v_add3_u32 v6, v6, v13, s76
	v_or_b32_e32 v13, s64, v12
	v_lshrrev_b32_e32 v15, 4, v28
	v_lshrrev_b32_e32 v40, 2, v28
	v_add3_u32 v5, v5, v14, s76
	v_lshrrev_b32_e32 v14, 1, v13
	v_xor_b32_e32 v15, v40, v15
	v_bfe_u32 v41, v2, 16, 1
	v_xor_b32_e32 v14, v14, v28
	v_lshlrev_b32_e32 v15, 5, v15
	v_lshlrev_b32_e32 v40, 3, v28
	v_mul_lo_u32 v13, v13, s5
	s_lshl_b32 s5, s82, 3
	v_pk_mul_f32 v[0:1], v[0:1], s[14:15] op_sel_hi:[1,0]
	v_add3_u32 v2, v2, v41, s76
	v_lshlrev_b32_e32 v14, 3, v14
	v_and_b32_e32 v15, 32, v15
	v_and_b32_e32 v41, 24, v40
	s_add_u32 s20, s3, s11
	v_bfe_u32 v42, v1, 16, 1
	v_and_or_b32 v14, v14, 56, v13
	v_or3_b32 v13, v41, v15, v13
	s_addc_u32 s21, s4, s10
	v_add3_u32 v1, v1, v42, s76
	v_lshlrev_b32_e32 v95, 1, v13
	v_lshlrev_b32_e32 v13, 2, v31
	v_lshrrev_b32_e32 v15, 1, v28
	v_bfe_u32 v41, v28, 1, 3
	v_bfe_u32 v42, v28, 2, 2
	v_and_b32_e32 v28, 16, v28
	s_add_u32 s22, s1, s11
	v_and_or_b32 v12, v12, 4, v42
	v_and_or_b32 v28, v13, 12, v28
	v_lshl_add_u32 v42, v29, 7, 0
	v_bitop3_b32 v15, v30, v15, 7 bitop3:0x78
	s_addc_u32 s23, s2, s10
	v_lshl_add_u32 v96, v15, 4, v42
	v_bitop3_b32 v15, v30, v41, 2 bitop3:0x36
	v_or_b32_e32 v100, s65, v13
	v_lshlrev_b32_e32 v12, 7, v12
	v_lshlrev_b32_e32 v13, 1, v28
	s_add_u32 s1, s47, s8
	v_lshl_add_u32 v97, v15, 4, v42
	v_bitop3_b32 v15, v30, v41, 4 bitop3:0x36
	v_add3_u32 v12, 0, v12, v13
	v_and_b32_e32 v13, 64, v40
	s_mov_b32 s3, 0xc000
	s_addc_u32 s2, s48, s9
	v_lshl_add_u32 v98, v15, 4, v42
	v_bitop3_b32 v15, v30, v41, 6 bitop3:0x36
	v_add3_u32 v101, v12, v13, s3
	v_bitop3_b32 v13, v40, 64, v40 bitop3:0xc
	s_add_u32 s24, s1, s5
	v_lshl_add_u32 v99, v15, 4, v42
	v_add3_u32 v102, v12, v13, s3
	s_addc_u32 s25, s2, 0
	s_add_i32 s85, s66, 0
	v_lshlrev_b32_e32 v104, 1, v14
	s_lshr_b32 s12, s83, 6
	s_mov_b32 m0, s85
	s_nop 0
	global_load_lds_dwordx4 v104, s[22:23]
	s_add_i32 s88, s85, 0xc000
	s_mov_b32 m0, s88
	s_nop 0
	global_load_lds_dwordx4 v95, s[20:21]
	s_add_u32 s2, s22, 0x70000
	s_cselect_b32 s98, 1, 0
	s_cmp_eq_u32 s101, 0
	s_cbranch_scc0 .Lmsk_skip_0
; #define LAS __attribute__((address_space(3)))
; #define ATT_ISSUE(st_, sl) do { _Pragma("unroll") for (int sb_ = 0; sb_ < NSUB; ++sb_) ATT_DMA(ATT_TILE((st_) * NSUB + sb_), sl, sb_); } while (0)
; #define ATT_BAR() asm volatile("s_waitcnt lgkmcnt(0)\n\ts_barrier" ::: "memory")
; template <int MODE, int DQK, int DV>
; __device__ __forceinline__ void attn_pass(LAS unsigned char* lds, const Tens& T, size_t rowbase, int q0, f32x16 (&o)[DV / 32], float& l_out, const int wave, QPre* qp = nullptr) {
;     ...
;     const int nvm = 1 + ((DQK == 96 && wave < 4) ? 1 : 0) + DV / 64 + ((MODE == AM_FOX && wave == 0) ? 1 : 0) + ((MODE == AM_DSA) ? 1 : 0);
;     ...
;     const unsigned koff = (unsigned)(r * 128), kswz = (unsigned)((r >> 1) & 7);
;     const unsigned roff = (unsigned)(8192 + r * 64), rswz = (unsigned)((r >> 2) & 3);
;     const int g16 = lane >> 4, qq = (lane & 15) >> 2, pp = lane & 3;
;     const int vsw = (DV == 64) ? ((qq >> 1) & 1) : qq;
;     const unsigned voff = (unsigned)((4 * (g16 >> 1) + qq) * VROW + (16 * (g16 & 1) + 4 * pp) * 2);
;     const LAS unsigned char* kfa[NSTEP]; const LAS unsigned char* vfa[NDB];
; #pragma unroll
;     for (int s = 0; s < NSTEP; ++s) {
;         kfa[s] = (s < 4) ? lds + OFF_K + koff + (((unsigned)(2 * s + h) ^ kswz) * 16) : lds + OFF_K + roff + (((unsigned)(2 * (s - 4) + h) ^ rswz) * 16);
;         asm volatile("" : "+v"(kfa[s]));
;     }
; #pragma unroll
;     for (int db = 0; db < NDB; ++db) { vfa[db] = lds + OFF_V + voff + (unsigned)((db ^ vsw) * 64); asm volatile("" : "+v"(vfa[db])); }
;     float m = -64.0f, l = 0.f;
;     bf16x8 kone = {0, 0, 0, 0, 0, 0, 0, 0}, qm = kone;
;     if (MODE == AM_DSA) { if (h == 0) { kone[0] = (short)0x3F80; kone[1] = (short)0x3F80; kone[2] = (short)0x3F80; } qm = split3_bf16(64.0f, h); }
;     f32x16 negm;
; #pragma unroll
;     for (int rg = 0; rg < 16; ++rg) negm[rg] = 64.0f;
; #pragma unroll
;     for (int i = 0; i < NDB; ++i) o[i] = f32x16{};
;     const int jlast = (q0 + wave * 32) / 64;
;     constexpr bool DESC = (MODE == AM_FOX);
;     ...
;     bool wdone = false;
;     volatile LAS int* dflag = (volatile LAS int*)(lds + OFF_MISC + 16);
;     const int nst = ntile / NSUB;
;     ATT_ISSUE(0, 0);
;     if (NRING == 3) ATT_ISSUE(1, 1);
;     if (NRING == 3) ATT_WAIT_PREV(); else asm volatile("s_waitcnt vmcnt(0)" ::: "memory");
;     ATT_BAR();
	s_add_i32 m0, s67, s100
	s_nop 0
	global_load_lds_dwordx4 v155, s[24:25]
.Lmsk_skip_0:
	s_cmp_lg_u32 s98, 0
	s_addc_u32 s3, s23, 0
	s_add_i32 s89, s85, 0x2000
	s_mov_b32 m0, s89
	s_nop 0
	global_load_lds_dwordx4 v104, s[2:3]
	s_add_u32 s2, s20, 0x70000
	s_addc_u32 s3, s21, 0
	s_add_i32 s91, s85, 0xe000
	s_mov_b32 m0, s91
	s_nop 0
	global_load_lds_dwordx4 v95, s[2:3]
	s_add_u32 s2, s24, 0x10000
	s_addc_u32 s3, s25, 0
	s_cselect_b32 s98, 1, 0
	s_cmp_eq_u32 s101, 1
	s_cbranch_scc0 .Lmsk_skip_1
	s_add_i32 m0, s68, s100
	s_nop 0
	global_load_lds_dwordx4 v155, s[2:3]
.Lmsk_skip_1:
	s_cmp_lg_u32 s98, 0
	s_add_u32 s2, s22, 0xe0000
	s_addc_u32 s3, s23, 0
	s_add_i32 s93, s85, 0x4000
	s_mov_b32 m0, s93
	s_nop 0
	global_load_lds_dwordx4 v104, s[2:3]
	s_add_u32 s2, s20, 0xe0000
	s_addc_u32 s3, s21, 0
	s_add_i32 s94, s85, 0x10000
	s_mov_b32 m0, s94
	s_nop 0
	global_load_lds_dwordx4 v95, s[2:3]
	s_add_u32 s2, s24, 0x20000
	s_addc_u32 s3, s25, 0
	s_cselect_b32 s98, 1, 0
	s_cmp_eq_u32 s101, 0
	s_cbranch_scc0 .Lmsk_skip_2
	s_add_i32 m0, s69, s100
	s_nop 0
	global_load_lds_dwordx4 v155, s[2:3]
.Lmsk_skip_2:
	s_cmp_lg_u32 s98, 0
	s_add_u32 s2, s22, 0x150000
	s_addc_u32 s3, s23, 0
	s_add_i32 s95, s85, 0x6000
	s_mov_b32 m0, s95
	s_nop 0
	global_load_lds_dwordx4 v104, s[2:3]
	s_add_u32 s2, s20, 0x150000
	s_addc_u32 s3, s21, 0
	s_add_i32 s96, s85, 0x12000
	v_pk_mul_f32 v[22:23], v[22:23], s[14:15] op_sel_hi:[1,0]
	s_mov_b32 m0, s96
	s_nop 0
	global_load_lds_dwordx4 v95, s[2:3]
	s_add_u32 s2, s24, 0x30000
	v_bfe_u32 v43, v23, 16, 1
	s_addc_u32 s3, s25, 0
	s_cselect_b32 s98, 1, 0
	s_cmp_eq_u32 s101, 1
	s_cbranch_scc0 .Lmsk_skip_3
	s_add_i32 m0, s70, s100
	s_nop 0
	global_load_lds_dwordx4 v155, s[2:3]
.Lmsk_skip_3:
	s_cmp_lg_u32 s98, 0
	v_add3_u32 v23, v23, v43, s76
	v_bfe_u32 v43, v0, 16, 1
	s_lshr_b32 s97, s0, 7
	s_add_i32 s8, s83, 0xffffff01
	s_add_i32 s1, s73, s82
	v_bfe_u32 v44, v22, 16, 1
	v_add3_u32 v0, v0, v43, s76
	s_waitcnt vmcnt(4)
	s_add_u32 s24, s24, 0x90000
	v_add3_u32 v22, v22, v44, s76
	s_waitcnt lgkmcnt(0)
	s_barrier
	v_or_b32_e32 v12, s90, v31
	v_perm_b32 v72, v17, v16, s78
	v_perm_b32 v84, v1, v0, s78
	v_add_u32_e32 v0, s1, v29
	s_addc_u32 s25, s25, 0
	s_lshr_b32 s0, s0, 6
	v_mov_b32_e32 v16, v66
	v_mov_b32_e32 v17, v66
	v_cmp_gt_u32_e64 s[2:3], 32, v31
	v_cmp_ne_u32_e64 s[4:5], 0, v12
	v_perm_b32 v75, v10, v20, s78
	v_perm_b32 v73, v19, v18, s78
	v_perm_b32 v79, v25, v24, s78
	v_perm_b32 v77, v23, v22, s78
	v_perm_b32 v76, v32, v21, s78
	v_perm_b32 v83, v37, v27, s78
	v_perm_b32 v82, v8, v9, s78
	v_perm_b32 v81, v11, v26, s78
	v_perm_b32 v87, v7, v6, s78
	v_perm_b32 v86, v5, v4, s78
	v_perm_b32 v85, v3, v2, s78
	v_sub_u32_e32 v110, v0, v106
	s_mul_i32 s0, s0, 0x70000
	v_mov_b32_e32 v18, v66
	v_mov_b32_e32 v19, v66
	v_mov_b32_e32 v20, v66
	v_mov_b32_e32 v21, v66
	v_mov_b32_e32 v22, v66
	v_mov_b32_e32 v23, v66
	v_mov_b32_e32 v24, v66
	v_mov_b32_e32 v25, v66
	v_mov_b32_e32 v26, v66
	v_mov_b32_e32 v27, v66
	v_mov_b32_e32 v28, v66
	v_mov_b32_e32 v29, v66
	v_mov_b32_e32 v30, v66
	v_mov_b32_e32 v31, v66
	v_mov_b64_e32 v[0:1], v[16:17]
	v_cndmask_b32_e64 v64, 0, v90, s[2:3]
	s_mov_b32 s10, 0
	v_cndmask_b32_e64 v69, 0, v91, s[2:3]
	v_cndmask_b32_e64 v68, 0, v92, s[2:3]
	v_perm_b32 v74, v33, v34, s78
	v_perm_b32 v78, v36, v35, s78
	v_perm_b32 v80, v38, v39, s78
	s_add_u32 s9, s0, 0xffd60000
	s_add_u32 s75, s0, 0xffe40000
	s_add_u32 s77, s0, 0xffc80000
	s_mov_b32 s11, 0
	v_mov_b64_e32 v[2:3], v[18:19]
	v_mov_b64_e32 v[4:5], v[20:21]
	v_mov_b64_e32 v[6:7], v[22:23]
	v_mov_b64_e32 v[8:9], v[24:25]
	v_mov_b64_e32 v[10:11], v[26:27]
	v_mov_b64_e32 v[12:13], v[28:29]
	v_mov_b64_e32 v[14:15], v[30:31]
	s_branch .LBB0_1621

; #define ATT_ISSUE(st_, sl) do { _Pragma("unroll") for (int sb_ = 0; sb_ < NSUB; ++sb_) ATT_DMA(ATT_TILE((st_) * NSUB + sb_), sl, sb_); } while (0)
; template <int MODE, int DQK, int DV>
; __device__ __forceinline__ void attn_pass(LAS unsigned char* lds, const Tens& T, size_t rowbase, int q0, f32x16 (&o)[DV / 32], float& l_out, const int wave, QPre* qp = nullptr) {
;     ...
;     auto tile_step = [&](auto slc_, const int st) __attribute__((always_inline)) -> bool {
;         constexpr int sl = decltype(slc_)::value;
;         { constexpr int sl2 = (sl + NRING - 1) % NRING; if (st + NRING - 1 < nst) ATT_ISSUE(st + NRING - 1, sl2); }
.LBB0_1621:
	s_add_i32 s0, s84, -2
	s_cmp_lt_u32 s0, s97
	s_cselect_b64 s[28:29], -1, 0
	s_cmp_ge_u32 s0, s97
	s_cselect_b64 s[30:31], -1, 0
	s_and_b64 vcc, exec, s[30:31]
	s_cbranch_vccnz .LBB0_1623
	s_add_u32 s15, s22, s26
	s_addc_u32 s33, s23, s27
	s_add_u32 s0, s15, 0x1c0000
	s_addc_u32 s1, s33, 0
	s_add_i32 s34, s85, 0x8000
	s_mov_b32 m0, s34
	s_nop 0
	global_load_lds_dwordx4 v104, s[0:1]
	s_add_u32 s34, s20, s26
	s_addc_u32 s35, s21, s27
	s_add_u32 s0, s34, 0x1c0000
	s_addc_u32 s1, s35, 0
	s_add_i32 s36, s85, 0x14000
	s_mov_b32 m0, s36
	s_nop 0
	global_load_lds_dwordx4 v95, s[0:1]
	s_add_u32 s0, s24, 0xfffb0000
	s_addc_u32 s1, s25, -1
	s_cselect_b32 s98, 1, 0
	s_cmp_eq_u32 s101, 0
	s_cbranch_scc0 .Lmsk_skip_4
	s_add_i32 m0, s71, s100
	s_nop 0
	global_load_lds_dwordx4 v155, s[0:1]
.Lmsk_skip_4:
	s_cmp_lg_u32 s98, 0
	s_add_u32 s0, s15, 0x230000
	s_addc_u32 s1, s33, 0
	s_add_i32 s15, s85, 0xa000
	s_mov_b32 m0, s15
	s_nop 0
	global_load_lds_dwordx4 v104, s[0:1]
	s_add_u32 s0, s34, 0x230000
	s_addc_u32 s1, s35, 0
	s_add_i32 s15, s85, 0x16000
	s_mov_b32 m0, s15
	s_nop 0
	global_load_lds_dwordx4 v95, s[0:1]
	s_add_u32 s0, s24, 0xfffc0000
	s_addc_u32 s1, s25, -1
	s_cselect_b32 s98, 1, 0
	s_cmp_eq_u32 s101, 1
	s_cbranch_scc0 .Lmsk_skip_5
	s_add_i32 m0, s72, s100
	s_nop 0
	global_load_lds_dwordx4 v155, s[0:1]
.Lmsk_skip_5:
	s_cmp_lg_u32 s98, 0

; #define ATT_ISSUE(st_, sl) do { _Pragma("unroll") for (int sb_ = 0; sb_ < NSUB; ++sb_) ATT_DMA(ATT_TILE((st_) * NSUB + sb_), sl, sb_); } while (0)
; #define ATT_WAIT_PREV() do { if (NSUB == 1) { if (nvm == 2) asm volatile("s_waitcnt vmcnt(2)" ::: "memory"); else asm volatile("s_waitcnt vmcnt(3)" ::: "memory"); } \
;                               else { if (nvm == 2) asm volatile("s_waitcnt vmcnt(4)" ::: "memory"); else asm volatile("s_waitcnt vmcnt(6)" ::: "memory"); } } while (0)
; #define ATT_BAR() asm volatile("s_waitcnt lgkmcnt(0)\n\ts_barrier" ::: "memory")
; template <int MODE, int DQK, int DV>
; __device__ __forceinline__ void attn_pass(LAS unsigned char* lds, const Tens& T, size_t rowbase, int q0, f32x16 (&o)[DV / 32], float& l_out, const int wave, QPre* qp = nullptr) {
;     ...
;     auto tile_step = [&](auto slc_, const int st) __attribute__((always_inline)) -> bool {
;         constexpr int sl = decltype(slc_)::value;
;         { constexpr int sl2 = (sl + NRING - 1) % NRING; if (st + NRING - 1 < nst) ATT_ISSUE(st + NRING - 1, sl2); }
;     ...
;         if (NRING == 3 && st + 2 < nst) ATT_WAIT_PREV(); else asm volatile("s_waitcnt vmcnt(0)" ::: "memory");
;         ATT_BAR();
.LBB0_1628:
	s_waitcnt vmcnt(4)
.LBB0_1629:
	s_waitcnt lgkmcnt(0)
	s_barrier
	s_add_i32 s0, s84, -3
	s_mov_b64 s[30:31], -1
	s_cmp_ge_u32 s0, s97
	s_nop 3
	v_readfirstlane_b32 s0, v0
	v_readfirstlane_b32 s1, v0
	v_readfirstlane_b32 s33, v0
	s_cbranch_scc1 .LBB0_1619
	s_add_i32 s15, s84, -1
	s_cmp_ge_u32 s15, s97
	s_cselect_b64 s[30:31], -1, 0
	s_and_b64 vcc, exec, s[30:31]
	s_cbranch_vccnz .LBB0_1632
	s_add_u32 s33, s22, s26
	s_addc_u32 s34, s23, s27
	s_add_u32 s0, s33, 0x2a0000
	s_addc_u32 s1, s34, 0
	s_mov_b32 m0, s85
	s_nop 0
	global_load_lds_dwordx4 v104, s[0:1]
	s_add_u32 s35, s20, s26
	s_addc_u32 s36, s21, s27
	s_add_u32 s0, s35, 0x2a0000
	s_addc_u32 s1, s36, 0
	s_mov_b32 m0, s88
	s_nop 0
	global_load_lds_dwordx4 v95, s[0:1]
	s_add_u32 s0, s24, 0xfffd0000
	s_addc_u32 s1, s25, -1
	s_cselect_b32 s98, 1, 0
	s_cmp_eq_u32 s101, 0
	s_cbranch_scc0 .Lmsk_skip_6
	s_add_i32 m0, s67, s100
	s_nop 0
	global_load_lds_dwordx4 v155, s[0:1]
.Lmsk_skip_6:
	s_cmp_lg_u32 s98, 0
	s_add_u32 s0, s33, 0x310000
	s_addc_u32 s1, s34, 0
	s_mov_b32 m0, s89
	s_nop 0
	global_load_lds_dwordx4 v104, s[0:1]
	s_add_u32 s0, s35, 0x310000
	s_addc_u32 s1, s36, 0
	s_mov_b32 m0, s91
	s_nop 0
	global_load_lds_dwordx4 v95, s[0:1]
	s_add_u32 s0, s24, 0xfffe0000
	s_addc_u32 s1, s25, -1
	s_cselect_b32 s98, 1, 0
	s_cmp_eq_u32 s101, 1
	s_cbranch_scc0 .Lmsk_skip_7
	s_add_i32 m0, s68, s100
	s_nop 0
	global_load_lds_dwordx4 v155, s[0:1]

; #define ATT_ISSUE(st_, sl) do { _Pragma("unroll") for (int sb_ = 0; sb_ < NSUB; ++sb_) ATT_DMA(ATT_TILE((st_) * NSUB + sb_), sl, sb_); } while (0)
; #define ATT_WAIT_PREV() do { if (NSUB == 1) { if (nvm == 2) asm volatile("s_waitcnt vmcnt(2)" ::: "memory"); else asm volatile("s_waitcnt vmcnt(3)" ::: "memory"); } \
;                               else { if (nvm == 2) asm volatile("s_waitcnt vmcnt(4)" ::: "memory"); else asm volatile("s_waitcnt vmcnt(6)" ::: "memory"); } } while (0)
; #define ATT_BAR() asm volatile("s_waitcnt lgkmcnt(0)\n\ts_barrier" ::: "memory")
; template <int MODE, int DQK, int DV>
; __device__ __forceinline__ void attn_pass(LAS unsigned char* lds, const Tens& T, size_t rowbase, int q0, f32x16 (&o)[DV / 32], float& l_out, const int wave, QPre* qp = nullptr) {
;     ...
;     auto tile_step = [&](auto slc_, const int st) __attribute__((always_inline)) -> bool {
;         constexpr int sl = decltype(slc_)::value;
;         { constexpr int sl2 = (sl + NRING - 1) % NRING; if (st + NRING - 1 < nst) ATT_ISSUE(st + NRING - 1, sl2); }
;     ...
;         if (NRING == 3 && st + 2 < nst) ATT_WAIT_PREV(); else asm volatile("s_waitcnt vmcnt(0)" ::: "memory");
;         ATT_BAR();
.LBB0_1638:
	s_waitcnt lgkmcnt(0)
	s_barrier
	s_mov_b64 s[30:31], -1
	s_nop 5
	v_readfirstlane_b32 s0, v0
	v_readfirstlane_b32 s1, v0
	s_andn2_b64 vcc, exec, s[28:29]
	v_readfirstlane_b32 s33, v0
	s_cbranch_vccnz .LBB0_1619
	s_cmp_ge_u32 s84, s97
	s_cselect_b64 s[28:29], -1, 0
	s_and_b64 vcc, exec, s[28:29]
	s_cbranch_vccnz .LBB0_1641
	s_add_u32 s30, s22, s26
	s_addc_u32 s31, s23, s27
	s_add_u32 s0, s30, 0x380000
	s_addc_u32 s1, s31, 0
	s_mov_b32 m0, s93
	s_nop 0
	global_load_lds_dwordx4 v104, s[0:1]
	s_add_u32 s33, s20, s26
	s_addc_u32 s34, s21, s27
	s_add_u32 s0, s33, 0x380000
	s_addc_u32 s1, s34, 0
	s_mov_b32 m0, s94
	s_nop 0
	global_load_lds_dwordx4 v95, s[0:1]
	s_add_u32 s0, s24, 0xffff0000
	s_addc_u32 s1, s25, -1
	s_cselect_b32 s98, 1, 0
	s_cmp_eq_u32 s101, 0
	s_cbranch_scc0 .Lmsk_skip_8
	s_add_i32 m0, s69, s100
	s_nop 0
	global_load_lds_dwordx4 v155, s[0:1]
.Lmsk_skip_8:
	s_cmp_lg_u32 s98, 0
	s_add_u32 s0, s30, 0x3f0000
	s_addc_u32 s1, s31, 0
	s_mov_b32 m0, s95
	s_nop 0
	global_load_lds_dwordx4 v104, s[0:1]
	s_add_u32 s0, s33, 0x3f0000
	s_addc_u32 s1, s34, 0
	s_mov_b32 m0, s96
	s_nop 0
	global_load_lds_dwordx4 v95, s[0:1]
	s_cselect_b32 s98, 1, 0
	s_cmp_eq_u32 s101, 1
	s_cbranch_scc0 .Lmsk_skip_9
	s_add_i32 m0, s70, s100
	s_nop 0
	global_load_lds_dwordx4 v155, s[24:25]
